# MoE-up full rounds: XCD owns 4 column tiles of 8 row tiles (variant b of the XCD-aware unit map)
# speedup vs baseline: 1.0138x; 1.0013x over previous
; __device__ __forceinline__ int otid() { int t = threadIdx.x; asm volatile("" : "+v"(t)); return t; }
;     __syncthreads();
;     const int tid = otid();
;     if (tid == 0) { int t = 0; for (int e = 0; e < 32; ++e) { tab[TAB_TPRE + e] = t; tab[TAB_OFFP + e] = t * 256; tab[TAB_CNT + e] = cnt[e]; t += (cnt[e] + 255) >> 8; } tab[TAB_TPRE + 32] = t; tab[TAB_OFFP + 32] = t * 256; }
;     __syncthreads();
;     if (ntn > 0 && tid < 32) {
;         const int total = tab[TAB_TPRE + 32] * ntn; int v = -1;
;         int Lx = tid * G + c;
;         if (ntn == 4 && G == 256) { const int x = c & 7, j = c >> 3; Lx = (tid * 64 + x * 8 + (j >> 2)) * 4 + (j & 3); }
;         if (Lx < total) { const int tile = Lx / ntn, pn = Lx % ntn; int e = 0; for (int k = 1; k < 32; ++k) e += (tab[TAB_TPRE + k] <= tile) ? 1 : 0; v = (e << 24) | ((tile - tab[TAB_TPRE + e]) << 8) | pn; }
;         tab[TAB_UNIT + tid] = v; tab[TAB_LX + tid] = Lx;
.LBB0_1661:
	s_or_b64 exec, exec, s[0:1]
	v_cmp_gt_i32_e32 vcc, 32, v1
	s_waitcnt lgkmcnt(0)
	s_barrier
	s_and_saveexec_b64 s[0:1], vcc
	s_cbranch_execz .LBB0_1665
	v_readlane_b32 s4, v254, 16
	s_nop 1
	v_mov_b32_e32 v2, s4
	ds_read_b32 v4, v2
	v_mul_lo_u32 v2, v1, s88
	s_bfe_u32 s72, s86, 0x20001
	s_lshl_b32 s72, s72, 6
	s_bfe_u32 s73, s86, 0x30005
	s_lshl_b32 s73, s73, 3
	s_or_b32 s72, s72, s73
	s_and_b32 s73, s86, 1
	s_lshl_b32 s73, s73, 2
	s_or_b32 s72, s72, s73
	s_bfe_u32 s73, s86, 0x20003
	s_or_b32 s72, s72, s73
	s_cmp_eq_u32 s88, 0x100
	s_cselect_b32 s72, s72, s86
	s_waitcnt lgkmcnt(0)
	v_lshlrev_b32_e32 v4, 3, v4
	v_add_u32_e32 v5, 0x100, v2
	v_cmp_gt_i32_e32 vcc, v5, v4
	v_mov_b32_e32 v6, s86
	v_mov_b32_e32 v7, s72
	s_nop 0
	v_cndmask_b32_e32 v6, v7, v6, vcc
	v_add_u32_e32 v2, v2, v6
	v_cmp_lt_i32_e32 vcc, v2, v4
	v_mov_b32_e32 v4, -1
	s_and_saveexec_b64 s[6:7], vcc
	s_cbranch_execz .LBB0_1664
	v_readlane_b32 s4, v254, 37
	v_ashrrev_i32_e32 v4, 31, v2
	v_lshrrev_b32_e32 v4, 29, v4
	v_mov_b32_e32 v6, s4
	ds_read2_b32 v[6:7], v6 offset1:1
	v_add_u32_e32 v5, v2, v4
	v_ashrrev_i32_e32 v4, 3, v5
	v_readlane_b32 s4, v254, 38
	v_and_b32_e32 v5, -8, v5
	s_waitcnt lgkmcnt(0)
	v_cmp_le_i32_e32 vcc, v6, v4
	v_mov_b32_e32 v6, s4
	v_readlane_b32 s4, v254, 39
	v_cndmask_b32_e64 v8, 0, 1, vcc
	v_cmp_le_i32_e32 vcc, v7, v4
	ds_read2_b32 v[6:7], v6 offset1:1
	v_sub_u32_e32 v5, v2, v5
	v_cndmask_b32_e64 v9, 0, 1, vcc
	s_waitcnt lgkmcnt(0)
	v_cmp_le_i32_e32 vcc, v6, v4
	s_nop 1
	v_addc_co_u32_e32 v8, vcc, v9, v8, vcc
	v_mov_b32_e32 v6, s4
	v_cmp_le_i32_e32 vcc, v7, v4
	ds_read2_b32 v[6:7], v6 offset1:1
	v_readlane_b32 s4, v254, 40
	v_cndmask_b32_e64 v9, 0, 1, vcc
	s_waitcnt lgkmcnt(0)
	v_cmp_le_i32_e32 vcc, v6, v4
	s_nop 1
	v_addc_co_u32_e32 v8, vcc, v8, v9, vcc
	v_mov_b32_e32 v6, s4
	v_cmp_le_i32_e32 vcc, v7, v4
	ds_read2_b32 v[6:7], v6 offset1:1
	v_readlane_b32 s4, v254, 41
	v_cndmask_b32_e64 v9, 0, 1, vcc
	s_waitcnt lgkmcnt(0)
	v_cmp_le_i32_e32 vcc, v6, v4
	s_nop 1
	v_addc_co_u32_e32 v8, vcc, v8, v9, vcc
	v_mov_b32_e32 v6, s4
	v_cmp_le_i32_e32 vcc, v7, v4
	ds_read2_b32 v[6:7], v6 offset1:1
	v_readlane_b32 s4, v254, 42
	v_cndmask_b32_e64 v9, 0, 1, vcc
	s_waitcnt lgkmcnt(0)
	v_cmp_le_i32_e32 vcc, v6, v4
	s_nop 1
	v_addc_co_u32_e32 v8, vcc, v8, v9, vcc
	v_mov_b32_e32 v6, s4
	v_cmp_le_i32_e32 vcc, v7, v4
	ds_read2_b32 v[6:7], v6 offset1:1
	v_readlane_b32 s4, v254, 43
	v_cndmask_b32_e64 v9, 0, 1, vcc
	s_waitcnt lgkmcnt(0)
	v_cmp_le_i32_e32 vcc, v6, v4
	s_nop 1
	v_addc_co_u32_e32 v8, vcc, v8, v9, vcc
	v_mov_b32_e32 v6, s4
	v_cmp_le_i32_e32 vcc, v7, v4
	ds_read2_b32 v[6:7], v6 offset1:1
	v_readlane_b32 s4, v254, 44
	v_cndmask_b32_e64 v9, 0, 1, vcc
	s_waitcnt lgkmcnt(0)
	v_cmp_le_i32_e32 vcc, v6, v4
	s_nop 1
	v_addc_co_u32_e32 v8, vcc, v8, v9, vcc
	v_mov_b32_e32 v6, s4
	v_cmp_le_i32_e32 vcc, v7, v4
	ds_read2_b32 v[6:7], v6 offset1:1
	v_readlane_b32 s4, v254, 45
	v_cndmask_b32_e64 v9, 0, 1, vcc
	s_waitcnt lgkmcnt(0)
	v_cmp_le_i32_e32 vcc, v6, v4
	s_nop 1
	v_addc_co_u32_e32 v8, vcc, v8, v9, vcc
	v_mov_b32_e32 v6, s4
	v_cmp_le_i32_e32 vcc, v7, v4
	ds_read2_b32 v[6:7], v6 offset1:1
	v_readlane_b32 s4, v254, 46
	v_cndmask_b32_e64 v9, 0, 1, vcc
	s_waitcnt lgkmcnt(0)
	v_cmp_le_i32_e32 vcc, v6, v4
	s_nop 1
	v_addc_co_u32_e32 v8, vcc, v8, v9, vcc
	v_mov_b32_e32 v6, s4
	v_cmp_le_i32_e32 vcc, v7, v4
	ds_read2_b32 v[6:7], v6 offset1:1
	v_readlane_b32 s4, v254, 47
	v_cndmask_b32_e64 v9, 0, 1, vcc
	s_waitcnt lgkmcnt(0)
	v_cmp_le_i32_e32 vcc, v6, v4
	s_nop 1
	v_addc_co_u32_e32 v8, vcc, v8, v9, vcc
	v_mov_b32_e32 v6, s4
	v_cmp_le_i32_e32 vcc, v7, v4
	ds_read2_b32 v[6:7], v6 offset1:1
	v_readlane_b32 s4, v254, 48
	v_cndmask_b32_e64 v9, 0, 1, vcc
	s_waitcnt lgkmcnt(0)
	v_cmp_le_i32_e32 vcc, v6, v4
	s_nop 1
	v_addc_co_u32_e32 v8, vcc, v8, v9, vcc
	v_mov_b32_e32 v6, s4
	v_cmp_le_i32_e32 vcc, v7, v4
	ds_read2_b32 v[6:7], v6 offset1:1
	v_readlane_b32 s4, v254, 49
	v_cndmask_b32_e64 v9, 0, 1, vcc
	s_waitcnt lgkmcnt(0)
	v_cmp_le_i32_e32 vcc, v6, v4
	s_nop 1
	v_addc_co_u32_e32 v8, vcc, v8, v9, vcc
	v_mov_b32_e32 v6, s4
	v_cmp_le_i32_e32 vcc, v7, v4
	ds_read2_b32 v[6:7], v6 offset1:1
	v_readlane_b32 s4, v254, 50
	v_cndmask_b32_e64 v9, 0, 1, vcc
	s_waitcnt lgkmcnt(0)
	v_cmp_le_i32_e32 vcc, v6, v4
	s_nop 1
	v_addc_co_u32_e32 v8, vcc, v8, v9, vcc
	v_mov_b32_e32 v6, s4
	v_cmp_le_i32_e32 vcc, v7, v4
	ds_read2_b32 v[6:7], v6 offset1:1
	v_readlane_b32 s4, v254, 51
	v_cndmask_b32_e64 v9, 0, 1, vcc
	s_waitcnt lgkmcnt(0)
	v_cmp_le_i32_e32 vcc, v6, v4
	s_nop 1
	v_addc_co_u32_e32 v8, vcc, v8, v9, vcc
	v_mov_b32_e32 v6, s4
	v_cmp_le_i32_e32 vcc, v7, v4
	ds_read2_b32 v[6:7], v6 offset1:1
	v_readlane_b32 s4, v254, 52
	v_cndmask_b32_e64 v9, 0, 1, vcc
	s_waitcnt lgkmcnt(0)
	v_cmp_le_i32_e32 vcc, v6, v4
	s_nop 1
	v_addc_co_u32_e32 v6, vcc, v8, v9, vcc
	v_mov_b32_e32 v8, s4
	ds_read_b32 v8, v8
	v_cmp_le_i32_e32 vcc, v7, v4
	s_nop 1
	v_cndmask_b32_e64 v7, 0, 1, vcc
	s_waitcnt lgkmcnt(0)
	v_cmp_le_i32_e32 vcc, v8, v4
	s_nop 1
	v_addc_co_u32_e32 v6, vcc, v6, v7, vcc
	v_lshlrev_b32_e32 v7, 24, v6
	v_lshl_add_u32 v6, v6, 2, 0
	v_add_u32_e32 v6, 0x20000, v6
	ds_read_b32 v6, v6
	s_waitcnt lgkmcnt(0)
	v_sub_u32_e32 v4, v4, v6
	v_lshlrev_b32_e32 v4, 8, v4
	v_or3_b32 v4, v4, v5, v7
